# P8 epilogue: slot words fully waited once up front, the later per-word waits (which only drained the scattered stores) removed
# speedup vs baseline: 1.0018x; 1.0018x over previous
.LBB0_983:
	s_or_b64 exec, exec, s[34:35]
	v_or_b32_e32 v26, 32, v4
	v_ashrrev_i32_e32 v27, 31, v26
	v_lshlrev_b64 v[26:27], 9, v[26:27]
	v_or_b32_e32 v28, v24, v25
	v_lshl_add_u64 v[26:27], s[10:11], 0, v[26:27]
	v_cmp_ne_u32_e32 vcc, 0, v28
	s_and_saveexec_b64 s[34:35], vcc
	s_cbranch_execz .LBB0_993
	v_cmp_ne_u32_sdwa s[38:39], v24, v169 src0_sel:BYTE_0 src1_sel:DWORD
	s_and_saveexec_b64 s[36:37], s[38:39]
	s_cbranch_execnz .LBB0_1134
	s_or_b64 exec, exec, s[36:37]
	v_cmp_ne_u32_sdwa s[38:39], v24, v169 src0_sel:BYTE_1 src1_sel:DWORD
	s_and_saveexec_b64 s[36:37], s[38:39]
	s_cbranch_execnz .LBB0_1135

.LBB0_993:
	s_or_b64 exec, exec, s[34:35]
	v_or_b32_e32 v24, v22, v23
	v_cmp_ne_u32_e32 vcc, 0, v24
	s_and_saveexec_b64 s[34:35], vcc
	s_cbranch_execz .LBB0_1003
	v_cmp_ne_u32_sdwa s[38:39], v22, v169 src0_sel:BYTE_0 src1_sel:DWORD
	s_and_saveexec_b64 s[36:37], s[38:39]
	s_cbranch_execnz .LBB0_1141
	s_or_b64 exec, exec, s[36:37]
	v_cmp_ne_u32_sdwa s[38:39], v22, v169 src0_sel:BYTE_1 src1_sel:DWORD
	s_and_saveexec_b64 s[36:37], s[38:39]
	s_cbranch_execnz .LBB0_1142

.LBB0_1003:
	s_or_b64 exec, exec, s[34:35]
	v_or_b32_e32 v22, 48, v4
	v_ashrrev_i32_e32 v23, 31, v22
	v_lshlrev_b64 v[22:23], 9, v[22:23]
	v_or_b32_e32 v24, v20, v21
	v_lshl_add_u64 v[22:23], s[10:11], 0, v[22:23]
	v_cmp_ne_u32_e32 vcc, 0, v24
	s_and_saveexec_b64 s[34:35], vcc
	s_cbranch_execz .LBB0_1013
	v_cmp_ne_u32_sdwa s[38:39], v20, v169 src0_sel:BYTE_0 src1_sel:DWORD
	s_and_saveexec_b64 s[36:37], s[38:39]
	s_cbranch_execnz .LBB0_1148
	s_or_b64 exec, exec, s[36:37]
	v_cmp_ne_u32_sdwa s[38:39], v20, v169 src0_sel:BYTE_1 src1_sel:DWORD
	s_and_saveexec_b64 s[36:37], s[38:39]
	s_cbranch_execnz .LBB0_1149

.LBB0_1013:
	s_or_b64 exec, exec, s[34:35]
	v_or_b32_e32 v20, v18, v19
	v_cmp_ne_u32_e32 vcc, 0, v20
	s_and_saveexec_b64 s[34:35], vcc
	s_cbranch_execz .LBB0_1023
	v_cmp_ne_u32_sdwa s[38:39], v18, v169 src0_sel:BYTE_0 src1_sel:DWORD
	s_and_saveexec_b64 s[36:37], s[38:39]
	s_cbranch_execnz .LBB0_1155
	s_or_b64 exec, exec, s[36:37]
	v_cmp_ne_u32_sdwa s[38:39], v18, v169 src0_sel:BYTE_1 src1_sel:DWORD
	s_and_saveexec_b64 s[36:37], s[38:39]
	s_cbranch_execnz .LBB0_1156

.LBB0_1023:
	s_or_b64 exec, exec, s[34:35]
	v_lshlrev_b64 v[18:19], 9, v[4:5]
	v_lshl_add_u64 v[18:19], s[10:11], 0, v[18:19]
	v_or_b32_e32 v20, v16, v17
	v_lshl_add_u64 v[18:19], v[18:19], 0, s[16:17]
	v_cmp_ne_u32_e32 vcc, 0, v20
	s_and_saveexec_b64 s[34:35], vcc
	s_cbranch_execz .LBB0_1033
	v_cmp_ne_u32_sdwa s[38:39], v16, v169 src0_sel:BYTE_0 src1_sel:DWORD
	s_and_saveexec_b64 s[36:37], s[38:39]
	s_cbranch_execnz .LBB0_1162
	s_or_b64 exec, exec, s[36:37]
	v_cmp_ne_u32_sdwa s[38:39], v16, v169 src0_sel:BYTE_1 src1_sel:DWORD
	s_and_saveexec_b64 s[36:37], s[38:39]
	s_cbranch_execnz .LBB0_1163

.LBB0_1033:
	s_or_b64 exec, exec, s[34:35]
	v_or_b32_e32 v16, v14, v15
	v_cmp_ne_u32_e32 vcc, 0, v16
	s_and_saveexec_b64 s[34:35], vcc
	s_cbranch_execz .LBB0_1043
	v_cmp_ne_u32_sdwa s[38:39], v14, v169 src0_sel:BYTE_0 src1_sel:DWORD
	s_and_saveexec_b64 s[36:37], s[38:39]
	s_cbranch_execnz .LBB0_1169
	s_or_b64 exec, exec, s[36:37]
	v_cmp_ne_u32_sdwa s[38:39], v14, v169 src0_sel:BYTE_1 src1_sel:DWORD
	s_and_saveexec_b64 s[36:37], s[38:39]
	s_cbranch_execnz .LBB0_1170

.LBB0_1043:
	s_or_b64 exec, exec, s[34:35]
	v_lshlrev_b64 v[14:15], 9, v[4:5]
	v_lshl_add_u64 v[14:15], s[10:11], 0, v[14:15]
	v_or_b32_e32 v16, v12, v13
	v_lshl_add_u64 v[14:15], v[14:15], 0, s[18:19]
	v_cmp_ne_u32_e32 vcc, 0, v16
	s_and_saveexec_b64 s[34:35], vcc
	s_cbranch_execz .LBB0_1053
	v_cmp_ne_u32_sdwa s[38:39], v12, v169 src0_sel:BYTE_0 src1_sel:DWORD
	s_and_saveexec_b64 s[36:37], s[38:39]
	s_cbranch_execnz .LBB0_1176
	s_or_b64 exec, exec, s[36:37]
	v_cmp_ne_u32_sdwa s[38:39], v12, v169 src0_sel:BYTE_1 src1_sel:DWORD
	s_and_saveexec_b64 s[36:37], s[38:39]
	s_cbranch_execnz .LBB0_1177

.LBB0_1053:
	s_or_b64 exec, exec, s[34:35]
	v_or_b32_e32 v12, v10, v11
	v_cmp_ne_u32_e32 vcc, 0, v12
	s_and_saveexec_b64 s[34:35], vcc
	s_cbranch_execz .LBB0_1063
	v_cmp_ne_u32_sdwa s[38:39], v10, v169 src0_sel:BYTE_0 src1_sel:DWORD
	s_and_saveexec_b64 s[36:37], s[38:39]
	s_cbranch_execnz .LBB0_1183
	s_or_b64 exec, exec, s[36:37]
	v_cmp_ne_u32_sdwa s[38:39], v10, v169 src0_sel:BYTE_1 src1_sel:DWORD
	s_and_saveexec_b64 s[36:37], s[38:39]
	s_cbranch_execnz .LBB0_1184

.LBB0_1063:
	s_or_b64 exec, exec, s[34:35]
	v_lshlrev_b64 v[10:11], 9, v[4:5]
	v_lshl_add_u64 v[10:11], s[10:11], 0, v[10:11]
	v_or_b32_e32 v12, v8, v9
	v_lshl_add_u64 v[10:11], v[10:11], 0, s[20:21]
	v_cmp_ne_u32_e32 vcc, 0, v12
	s_and_saveexec_b64 s[34:35], vcc
	s_cbranch_execz .LBB0_1073
	v_cmp_ne_u32_sdwa s[38:39], v8, v169 src0_sel:BYTE_0 src1_sel:DWORD
	s_and_saveexec_b64 s[36:37], s[38:39]
	s_cbranch_execnz .LBB0_1190
	s_or_b64 exec, exec, s[36:37]
	v_cmp_ne_u32_sdwa s[38:39], v8, v169 src0_sel:BYTE_1 src1_sel:DWORD
	s_and_saveexec_b64 s[36:37], s[38:39]
	s_cbranch_execnz .LBB0_1191

.LBB0_1073:
	s_or_b64 exec, exec, s[34:35]
	v_or_b32_e32 v8, v6, v7
	v_cmp_ne_u32_e32 vcc, 0, v8
	s_and_saveexec_b64 s[34:35], vcc
	s_cbranch_execz .LBB0_1083
	v_cmp_ne_u32_sdwa s[38:39], v6, v169 src0_sel:BYTE_0 src1_sel:DWORD
	s_and_saveexec_b64 s[36:37], s[38:39]
	s_cbranch_execnz .LBB0_1197
	s_or_b64 exec, exec, s[36:37]
	v_cmp_ne_u32_sdwa s[38:39], v6, v169 src0_sel:BYTE_1 src1_sel:DWORD
	s_and_saveexec_b64 s[36:37], s[38:39]
	s_cbranch_execnz .LBB0_1198

.LBB0_1083:
	s_or_b64 exec, exec, s[34:35]
	v_lshlrev_b64 v[4:5], 9, v[4:5]
	v_lshl_add_u64 v[4:5], s[10:11], 0, v[4:5]
	v_or_b32_e32 v6, v2, v3
	v_lshl_add_u64 v[4:5], v[4:5], 0, s[22:23]
	v_cmp_ne_u32_e32 vcc, 0, v6
	s_and_saveexec_b64 s[34:35], vcc
	s_cbranch_execz .LBB0_1093
	v_cmp_ne_u32_sdwa s[38:39], v2, v169 src0_sel:BYTE_0 src1_sel:DWORD
	s_and_saveexec_b64 s[36:37], s[38:39]
	s_cbranch_execnz .LBB0_1204
	s_or_b64 exec, exec, s[36:37]
	v_cmp_ne_u32_sdwa s[38:39], v2, v169 src0_sel:BYTE_1 src1_sel:DWORD
	s_and_saveexec_b64 s[36:37], s[38:39]
	s_cbranch_execnz .LBB0_1205

.LBB0_1093:
	s_or_b64 exec, exec, s[34:35]
	v_or_b32_e32 v2, v0, v1
	v_cmp_ne_u32_e32 vcc, 0, v2
	s_and_saveexec_b64 s[34:35], vcc
	s_cbranch_execz .LBB0_1103
	v_cmp_ne_u32_sdwa s[38:39], v0, v169 src0_sel:BYTE_0 src1_sel:DWORD
	s_and_saveexec_b64 s[36:37], s[38:39]
	s_cbranch_execnz .LBB0_1211
	s_or_b64 exec, exec, s[36:37]
	v_cmp_ne_u32_sdwa s[38:39], v0, v169 src0_sel:BYTE_1 src1_sel:DWORD
	s_and_saveexec_b64 s[36:37], s[38:39]
	s_cbranch_execnz .LBB0_1212
